# v59 + GQA fast path: the two K pieces of tile j+2 written to LDS inside the P.V segment, only the V pieces stay behind the mid-step barrier
# speedup vs baseline: 1.0044x; 1.0044x over previous
.LBB0_881:
	ds_read_b128 v[96:99], v216 offset:49152
	ds_read_b128 v[100:103], v216 offset:57344
	ds_read_b128 v[178:181], v218 offset:49152
	ds_read_b128 v[182:185], v218 offset:57344
	ds_read_b128 v[240:243], v219 offset:49152
	ds_read_b128 v[244:247], v219 offset:57344
	v_add_f32_e32 v88, v64, v65
	v_add_f32_e32 v89, v72, v73
	v_add_f32_e32 v90, v80, v81
	v_add_f32_e32 v91, v194, v195
	v_add_f32_e32 v88, v66, v88
	v_add_f32_e32 v89, v74, v89
	v_add_f32_e32 v90, v82, v90
	s_waitcnt lgkmcnt(4)
	v_mfma_f32_32x32x16_bf16 v[112:127], v[96:99], v[138:141], 0
	v_mfma_f32_32x32x16_bf16 v[96:111], v[100:103], v[138:141], 0
	v_add_f32_e32 v91, v196, v91
	v_add_f32_e32 v88, v67, v88
	v_add_f32_e32 v89, v75, v89
	v_add_f32_e32 v90, v83, v90
	v_add_f32_e32 v91, v197, v91
	v_add_f32_e32 v88, v68, v88
	v_add_f32_e32 v89, v76, v89
	s_waitcnt lgkmcnt(2)
	v_mfma_f32_32x32x16_bf16 v[112:127], v[178:181], v[154:157], v[112:127]
	v_mfma_f32_32x32x16_bf16 v[96:111], v[182:185], v[154:157], v[96:111]
	ds_read_b128 v[178:181], v220 offset:49152
	ds_read_b128 v[182:185], v220 offset:57344
	v_add_f32_e32 v90, v84, v90
	v_add_f32_e32 v91, v92, v91
	v_add_f32_e32 v88, v69, v88
	v_add_f32_e32 v89, v77, v89
	v_add_f32_e32 v90, v85, v90
	v_add_f32_e32 v91, v93, v91
	v_add_f32_e32 v88, v70, v88
	s_waitcnt lgkmcnt(2)
	v_mfma_f32_32x32x16_bf16 v[112:127], v[240:243], v[158:161], v[112:127]
	v_mfma_f32_32x32x16_bf16 v[96:111], v[244:247], v[158:161], v[96:111]
	ds_read_b128 v[240:243], v221 offset:49152
	ds_read_b128 v[244:247], v221 offset:57344
	v_add_f32_e32 v89, v78, v89
	v_add_f32_e32 v90, v86, v90
	v_add_f32_e32 v91, v94, v91
	v_add_f32_e32 v88, v71, v88
	v_add_f32_e32 v89, v79, v89
	v_add_f32_e32 v90, v87, v90
	v_add_f32_e32 v91, v95, v91
	s_waitcnt lgkmcnt(2)
	v_mfma_f32_32x32x16_bf16 v[112:127], v[178:181], v[150:153], v[112:127]
	v_mfma_f32_32x32x16_bf16 v[96:111], v[182:185], v[150:153], v[96:111]
	ds_read_b128 v[178:181], v222 offset:49152
	ds_read_b128 v[182:185], v222 offset:57344
	v_add_f32_e32 v88, v89, v88
	v_add_f32_e32 v89, v91, v90
	v_add_f32_e32 v227, v88, v89
	v_cvt_pk_bf16_f32 v88, v64, v65
	v_cvt_pk_bf16_f32 v89, v66, v67
	v_cvt_pk_bf16_f32 v90, v68, v69
	v_cvt_pk_bf16_f32 v91, v70, v71
	s_waitcnt lgkmcnt(2)
	v_mfma_f32_32x32x16_bf16 v[112:127], v[240:243], v[146:149], v[112:127]
	v_mfma_f32_32x32x16_bf16 v[96:111], v[244:247], v[146:149], v[96:111]
	ds_read_b128 v[240:243], v224 offset:49152
	ds_read_b128 v[244:247], v224 offset:57344
	v_cvt_pk_bf16_f32 v72, v72, v73
	v_cvt_pk_bf16_f32 v73, v74, v75
	v_cvt_pk_bf16_f32 v74, v76, v77
	v_cvt_pk_bf16_f32 v75, v78, v79
	s_waitcnt lgkmcnt(2)
	v_mfma_f32_32x32x16_bf16 v[112:127], v[178:181], v[142:145], v[112:127]
	v_mfma_f32_32x32x16_bf16 v[96:111], v[182:185], v[142:145], v[96:111]
	ds_read_b128 v[178:181], v223 offset:49152
	ds_read_b128 v[182:185], v223 offset:57344
	v_cvt_pk_bf16_f32 v64, v80, v81
	v_cvt_pk_bf16_f32 v65, v82, v83
	v_cvt_pk_bf16_f32 v66, v84, v85
	v_cvt_pk_bf16_f32 v67, v86, v87
	v_cvt_pk_bf16_f32 v68, v194, v195
	v_cvt_pk_bf16_f32 v69, v196, v197
	v_cvt_pk_bf16_f32 v70, v92, v93
	s_waitcnt lgkmcnt(2)
	v_mfma_f32_32x32x16_bf16 v[112:127], v[240:243], v[134:137], v[112:127]
	v_mfma_f32_32x32x16_bf16 v[96:111], v[244:247], v[134:137], v[96:111]
	v_cvt_pk_bf16_f32 v71, v94, v95
	s_waitcnt lgkmcnt(0)
	v_mfma_f32_32x32x16_bf16 v[112:127], v[178:181], v[130:133], v[112:127]
	v_mfma_f32_32x32x16_bf16 v[96:111], v[182:185], v[130:133], v[96:111]
	s_add_i32 s2, s39, -1
	s_mul_i32 s2, s2, s62
	s_lshl_b32 s72, s2, 6
	s_lshl_b64 s[2:3], s[72:73], 1
	s_add_u32 s12, s10, s2
	s_addc_u32 s13, s11, s3
	s_add_u32 s2, s8, s2
	s_addc_u32 s3, s9, s3
	global_load_dwordx4 v[178:181], v128, s[12:13]
	global_load_dwordx4 v[182:185], v198, s[12:13]
	global_load_dwordx4 v[186:189], v128, s[2:3]
	global_load_dwordx4 v[190:193], v198, s[2:3]
	ds_read_b64_tr_b16 v[76:77], v209 offset:0
	ds_read_b64_tr_b16 v[78:79], v209 offset:0x800
	ds_read_b64_tr_b16 v[80:81], v209 offset:0x1000
	ds_read_b64_tr_b16 v[82:83], v209 offset:0x1800
	ds_read_b64_tr_b16 v[84:85], v209 offset:0x2000
	ds_read_b64_tr_b16 v[86:87], v209 offset:0x2800
	ds_read_b64_tr_b16 v[92:93], v209 offset:0x3000
	ds_read_b64_tr_b16 v[94:95], v209 offset:0x3800
	s_waitcnt lgkmcnt(0)
	s_nop 0
	v_mfma_f32_32x32x16_bf16 v[0:15], v[76:79], v[88:91], v[0:15]
	v_mfma_f32_32x32x16_bf16 v[0:15], v[80:83], v[72:75], v[0:15]
	v_mfma_f32_32x32x16_bf16 v[0:15], v[84:87], v[64:67], v[0:15]
	ds_read_b64_tr_b16 v[76:77], v209 offset:0x200
	ds_read_b64_tr_b16 v[78:79], v209 offset:0xa00
	ds_read_b64_tr_b16 v[80:81], v209 offset:0x1200
	v_mfma_f32_32x32x16_bf16 v[0:15], v[92:95], v[68:71], v[0:15]
	s_waitcnt vmcnt(4)
	ds_write_b128 v214, v[170:173] offset:32768
	ds_write_b128 v215, v[174:177] offset:32768
	ds_read_b64_tr_b16 v[82:83], v209 offset:0x1a00
	ds_read_b64_tr_b16 v[84:85], v209 offset:0x2200
	ds_read_b64_tr_b16 v[86:87], v209 offset:0x2a00
	ds_read_b64_tr_b16 v[92:93], v209 offset:0x3200
	ds_read_b64_tr_b16 v[94:95], v209 offset:0x3a00
	s_waitcnt lgkmcnt(0)
	v_mfma_f32_32x32x16_bf16 v[48:63], v[76:79], v[88:91], v[48:63]
	v_mfma_f32_32x32x16_bf16 v[48:63], v[80:83], v[72:75], v[48:63]
	v_mfma_f32_32x32x16_bf16 v[48:63], v[84:87], v[64:67], v[48:63]
	ds_read_b64_tr_b16 v[76:77], v209 offset:0x400
	ds_read_b64_tr_b16 v[78:79], v209 offset:0xc00
	ds_read_b64_tr_b16 v[80:81], v209 offset:0x1400
	ds_read_b64_tr_b16 v[82:83], v209 offset:0x1c00
	v_mfma_f32_32x32x16_bf16 v[48:63], v[92:95], v[68:71], v[48:63]
	ds_read_b64_tr_b16 v[84:85], v209 offset:0x2400
	ds_read_b64_tr_b16 v[86:87], v209 offset:0x2c00
	ds_read_b64_tr_b16 v[92:93], v209 offset:0x3400
	ds_read_b64_tr_b16 v[94:95], v209 offset:0x3c00
	s_waitcnt lgkmcnt(0)
	v_mfma_f32_32x32x16_bf16 v[32:47], v[76:79], v[88:91], v[32:47]
	ds_read_b64_tr_b16 v[76:77], v209 offset:0x600
	ds_read_b64_tr_b16 v[78:79], v209 offset:0xe00
	v_exp_f32_e32 v234, v104
	v_exp_f32_e32 v235, v105
	v_exp_f32_e32 v236, v106
	v_exp_f32_e32 v237, v107
	v_exp_f32_e32 v238, v108
	v_exp_f32_e32 v239, v109
	v_exp_f32_e32 v231, v110
	v_exp_f32_e32 v249, v111
	v_mfma_f32_32x32x16_bf16 v[32:47], v[80:83], v[72:75], v[32:47]
	v_exp_f32_e32 v80, v112
	v_exp_f32_e32 v81, v113
	v_exp_f32_e32 v82, v114
	v_exp_f32_e32 v83, v115
	v_mfma_f32_32x32x16_bf16 v[32:47], v[84:87], v[64:67], v[32:47]
	v_exp_f32_e32 v84, v116
	v_exp_f32_e32 v85, v117
	v_exp_f32_e32 v86, v118
	v_exp_f32_e32 v87, v119
	v_exp_f32_e32 v112, v96
	v_exp_f32_e32 v113, v97
	v_exp_f32_e32 v114, v98
	v_exp_f32_e32 v115, v99
	v_exp_f32_e32 v116, v100
	v_exp_f32_e32 v117, v101
	v_exp_f32_e32 v118, v102
	v_exp_f32_e32 v119, v103
	v_mfma_f32_32x32x16_bf16 v[32:47], v[92:95], v[68:71], v[32:47]
	ds_read_b64_tr_b16 v[92:93], v209 offset:0x1600
	ds_read_b64_tr_b16 v[94:95], v209 offset:0x1e00
	ds_read_b64_tr_b16 v[96:97], v209 offset:0x2600
	ds_read_b64_tr_b16 v[98:99], v209 offset:0x2e00
	ds_read_b64_tr_b16 v[100:101], v209 offset:0x3600
	ds_read_b64_tr_b16 v[102:103], v209 offset:0x3e00
	s_waitcnt lgkmcnt(0)
	v_mfma_f32_32x32x16_bf16 v[16:31], v[76:79], v[88:91], v[16:31]
	v_exp_f32_e32 v88, v120
	v_exp_f32_e32 v89, v121
	v_exp_f32_e32 v90, v122
	v_exp_f32_e32 v91, v123
	v_mfma_f32_32x32x16_bf16 v[16:31], v[92:95], v[72:75], v[16:31]
	v_exp_f32_e32 v92, v124
	v_exp_f32_e32 v93, v125
	v_exp_f32_e32 v94, v126
	v_exp_f32_e32 v95, v127
	s_barrier
	v_mfma_f32_32x32x16_bf16 v[16:31], v[96:99], v[64:67], v[16:31]
	ds_write_b128 v212, v[162:165]
	ds_write_b128 v213, v[166:169]
	v_mfma_f32_32x32x16_bf16 v[16:31], v[100:103], v[68:71], v[16:31]
.LBB0_883:
	s_waitcnt lgkmcnt(0)
	s_barrier
	ds_read_b128 v[64:67], v216 offset:32768
	ds_read_b128 v[68:71], v216 offset:40960
	ds_read_b128 v[162:165], v218 offset:32768
	ds_read_b128 v[166:169], v218 offset:40960
	ds_read_b128 v[240:243], v219 offset:32768
	ds_read_b128 v[244:247], v219 offset:40960
	v_add_f32_e32 v120, v80, v81
	v_add_f32_e32 v121, v88, v89
	v_add_f32_e32 v122, v112, v113
	v_add_f32_e32 v123, v234, v235
	v_add_f32_e32 v120, v82, v120
	v_add_f32_e32 v121, v90, v121
	v_add_f32_e32 v122, v114, v122
	s_waitcnt lgkmcnt(4)
	v_mfma_f32_32x32x16_bf16 v[96:111], v[64:67], v[138:141], 0
	v_mfma_f32_32x32x16_bf16 v[64:79], v[68:71], v[138:141], 0
	v_add_f32_e32 v123, v236, v123
	v_add_f32_e32 v120, v83, v120
	v_add_f32_e32 v121, v91, v121
	v_add_f32_e32 v122, v115, v122
	v_add_f32_e32 v123, v237, v123
	v_add_f32_e32 v120, v84, v120
	v_add_f32_e32 v121, v92, v121
	s_waitcnt lgkmcnt(2)
	v_mfma_f32_32x32x16_bf16 v[96:111], v[162:165], v[154:157], v[96:111]
	v_mfma_f32_32x32x16_bf16 v[64:79], v[166:169], v[154:157], v[64:79]
	ds_read_b128 v[162:165], v220 offset:32768
	ds_read_b128 v[166:169], v220 offset:40960
	v_add_f32_e32 v122, v116, v122
	v_add_f32_e32 v123, v238, v123
	v_add_f32_e32 v120, v85, v120
	v_add_f32_e32 v121, v93, v121
	v_add_f32_e32 v122, v117, v122
	v_add_f32_e32 v123, v239, v123
	v_add_f32_e32 v120, v86, v120
	s_waitcnt lgkmcnt(2)
	v_mfma_f32_32x32x16_bf16 v[96:111], v[240:243], v[158:161], v[96:111]
	v_mfma_f32_32x32x16_bf16 v[64:79], v[244:247], v[158:161], v[64:79]
	ds_read_b128 v[240:243], v221 offset:32768
	ds_read_b128 v[244:247], v221 offset:40960
	v_add_f32_e32 v121, v94, v121
	v_add_f32_e32 v122, v118, v122
	v_add_f32_e32 v123, v231, v123
	v_add_f32_e32 v120, v87, v120
	v_add_f32_e32 v121, v95, v121
	v_add_f32_e32 v122, v119, v122
	v_add_f32_e32 v123, v249, v123
	s_waitcnt lgkmcnt(2)
	v_mfma_f32_32x32x16_bf16 v[96:111], v[162:165], v[150:153], v[96:111]
	v_mfma_f32_32x32x16_bf16 v[64:79], v[166:169], v[150:153], v[64:79]
	ds_read_b128 v[162:165], v222 offset:32768
	ds_read_b128 v[166:169], v222 offset:40960
	v_add_f32_e32 v120, v121, v120
	v_add_f32_e32 v121, v123, v122
	v_add_f32_e32 v229, v120, v121
	v_cvt_pk_bf16_f32 v124, v80, v81
	v_cvt_pk_bf16_f32 v125, v82, v83
	v_cvt_pk_bf16_f32 v126, v84, v85
	s_waitcnt lgkmcnt(2)
	v_mfma_f32_32x32x16_bf16 v[96:111], v[240:243], v[146:149], v[96:111]
	v_mfma_f32_32x32x16_bf16 v[64:79], v[244:247], v[146:149], v[64:79]
	ds_read_b128 v[240:243], v224 offset:32768
	ds_read_b128 v[244:247], v224 offset:40960
	v_cvt_pk_bf16_f32 v127, v86, v87
	v_cvt_pk_bf16_f32 v120, v88, v89
	v_cvt_pk_bf16_f32 v121, v90, v91
	v_cvt_pk_bf16_f32 v122, v92, v93
	v_cvt_pk_bf16_f32 v123, v94, v95
	v_cvt_pk_bf16_f32 v112, v112, v113
	v_cvt_pk_bf16_f32 v113, v114, v115
	s_waitcnt lgkmcnt(2)
	v_mfma_f32_32x32x16_bf16 v[96:111], v[162:165], v[142:145], v[96:111]
	v_mfma_f32_32x32x16_bf16 v[64:79], v[166:169], v[142:145], v[64:79]
	ds_read_b128 v[162:165], v223 offset:32768
	ds_read_b128 v[166:169], v223 offset:40960
	v_cvt_pk_bf16_f32 v114, v116, v117
	v_cvt_pk_bf16_f32 v115, v118, v119
	v_cvt_pk_bf16_f32 v116, v234, v235
	v_cvt_pk_bf16_f32 v117, v236, v237
	v_cvt_pk_bf16_f32 v118, v238, v239
	v_cvt_pk_bf16_f32 v119, v231, v249
	s_waitcnt lgkmcnt(2)
	v_mfma_f32_32x32x16_bf16 v[96:111], v[240:243], v[134:137], v[96:111]
	v_mfma_f32_32x32x16_bf16 v[64:79], v[244:247], v[134:137], v[64:79]
	s_waitcnt lgkmcnt(0)
	v_mfma_f32_32x32x16_bf16 v[96:111], v[162:165], v[130:133], v[96:111]
	v_mfma_f32_32x32x16_bf16 v[64:79], v[166:169], v[130:133], v[64:79]
	s_min_i32 s2, s39, s14
	s_mul_i32 s2, s2, s62
	s_lshl_b32 s72, s2, 6
	s_lshl_b64 s[2:3], s[72:73], 1
	s_add_u32 s12, s10, s2
	s_addc_u32 s13, s11, s3
	s_add_u32 s2, s8, s2
	s_addc_u32 s3, s9, s3
	global_load_dwordx4 v[162:165], v128, s[12:13]
	global_load_dwordx4 v[166:169], v198, s[12:13]
	global_load_dwordx4 v[170:173], v128, s[2:3]
	global_load_dwordx4 v[174:177], v198, s[2:3]
	ds_read_b64_tr_b16 v[80:81], v211 offset:0
	ds_read_b64_tr_b16 v[82:83], v211 offset:0x800
	ds_read_b64_tr_b16 v[84:85], v211 offset:0x1000
	ds_read_b64_tr_b16 v[86:87], v211 offset:0x1800
	ds_read_b64_tr_b16 v[88:89], v211 offset:0x2000
	ds_read_b64_tr_b16 v[90:91], v211 offset:0x2800
	ds_read_b64_tr_b16 v[92:93], v211 offset:0x3000
	ds_read_b64_tr_b16 v[94:95], v211 offset:0x3800
	s_waitcnt lgkmcnt(0)
	s_nop 0
	v_mfma_f32_32x32x16_bf16 v[0:15], v[80:83], v[124:127], v[0:15]
	v_mfma_f32_32x32x16_bf16 v[0:15], v[84:87], v[120:123], v[0:15]
	v_mfma_f32_32x32x16_bf16 v[0:15], v[88:91], v[112:115], v[0:15]
	ds_read_b64_tr_b16 v[80:81], v211 offset:0x200
	ds_read_b64_tr_b16 v[82:83], v211 offset:0xa00
	ds_read_b64_tr_b16 v[84:85], v211 offset:0x1200
	v_mfma_f32_32x32x16_bf16 v[0:15], v[92:95], v[116:119], v[0:15]
	s_waitcnt vmcnt(4)
	ds_write_b128 v214, v[186:189] offset:49152
	ds_write_b128 v215, v[190:193] offset:49152
	ds_read_b64_tr_b16 v[86:87], v211 offset:0x1a00
	ds_read_b64_tr_b16 v[88:89], v211 offset:0x2200
	ds_read_b64_tr_b16 v[90:91], v211 offset:0x2a00
	ds_read_b64_tr_b16 v[92:93], v211 offset:0x3200
	ds_read_b64_tr_b16 v[94:95], v211 offset:0x3a00
	s_waitcnt lgkmcnt(0)
	v_mfma_f32_32x32x16_bf16 v[48:63], v[80:83], v[124:127], v[48:63]
	v_mfma_f32_32x32x16_bf16 v[48:63], v[84:87], v[120:123], v[48:63]
	v_mfma_f32_32x32x16_bf16 v[48:63], v[88:91], v[112:115], v[48:63]
	ds_read_b64_tr_b16 v[80:81], v211 offset:0x400
	ds_read_b64_tr_b16 v[82:83], v211 offset:0xc00
	ds_read_b64_tr_b16 v[84:85], v211 offset:0x1400
	ds_read_b64_tr_b16 v[86:87], v211 offset:0x1c00
	v_mfma_f32_32x32x16_bf16 v[48:63], v[92:95], v[116:119], v[48:63]
	ds_read_b64_tr_b16 v[88:89], v211 offset:0x2400
	ds_read_b64_tr_b16 v[90:91], v211 offset:0x2c00
	ds_read_b64_tr_b16 v[92:93], v211 offset:0x3400
	ds_read_b64_tr_b16 v[94:95], v211 offset:0x3c00
	s_waitcnt lgkmcnt(0)
	v_mfma_f32_32x32x16_bf16 v[32:47], v[80:83], v[124:127], v[32:47]
	v_exp_f32_e32 v80, v64
	v_exp_f32_e32 v81, v65
	v_exp_f32_e32 v64, v96
	v_exp_f32_e32 v65, v97
	v_exp_f32_e32 v82, v66
	v_exp_f32_e32 v83, v67
	v_exp_f32_e32 v66, v98
	v_exp_f32_e32 v67, v99
	v_mfma_f32_32x32x16_bf16 v[32:47], v[84:87], v[120:123], v[32:47]
	v_exp_f32_e32 v84, v68
	v_exp_f32_e32 v85, v69
	v_exp_f32_e32 v68, v100
	v_exp_f32_e32 v69, v101
	v_exp_f32_e32 v86, v70
	v_exp_f32_e32 v87, v71
	v_exp_f32_e32 v70, v102
	v_exp_f32_e32 v71, v103
	v_mfma_f32_32x32x16_bf16 v[32:47], v[88:91], v[112:115], v[32:47]
	v_exp_f32_e32 v194, v72
	v_exp_f32_e32 v195, v73
	ds_read_b64_tr_b16 v[72:73], v211 offset:0x600
	v_exp_f32_e32 v196, v74
	v_exp_f32_e32 v197, v75
	ds_read_b64_tr_b16 v[74:75], v211 offset:0xe00
	v_mfma_f32_32x32x16_bf16 v[32:47], v[92:95], v[116:119], v[32:47]
	v_exp_f32_e32 v92, v76
	v_exp_f32_e32 v93, v77
	ds_read_b64_tr_b16 v[76:77], v211 offset:0x1600
	v_exp_f32_e32 v94, v78
	v_exp_f32_e32 v95, v79
	ds_read_b64_tr_b16 v[78:79], v211 offset:0x1e00
	ds_read_b64_tr_b16 v[96:97], v211 offset:0x2600
	ds_read_b64_tr_b16 v[98:99], v211 offset:0x2e00
	ds_read_b64_tr_b16 v[100:101], v211 offset:0x3600
	ds_read_b64_tr_b16 v[102:103], v211 offset:0x3e00
	s_waitcnt lgkmcnt(0)
	v_mfma_f32_32x32x16_bf16 v[16:31], v[72:75], v[124:127], v[16:31]
	v_exp_f32_e32 v72, v104
	v_exp_f32_e32 v73, v105
	v_exp_f32_e32 v74, v106
	v_exp_f32_e32 v75, v107
	v_mfma_f32_32x32x16_bf16 v[16:31], v[76:79], v[120:123], v[16:31]
	v_exp_f32_e32 v76, v108
	v_exp_f32_e32 v77, v109
	v_exp_f32_e32 v78, v110
	v_exp_f32_e32 v79, v111
	s_barrier
	v_mfma_f32_32x32x16_bf16 v[16:31], v[96:99], v[112:115], v[16:31]
	ds_write_b128 v212, v[178:181] offset:16384
	ds_write_b128 v213, v[182:185] offset:16384
	v_mfma_f32_32x32x16_bf16 v[16:31], v[100:103], v[116:119], v[16:31]
